# band: bias LDS reads and P.V transposed reads issued in batches ahead of their consumers (counted lgkmcnt), 32-bit row-index updates; on top of v28
# baseline (speedup 1.0000x reference)
.LBB0_1265:
	s_waitcnt vmcnt(0)
	v_mfma_f32_32x32x16_bf16 v[52:67], v[144:147], v[124:127], 0
	ds_write_b128 v191, v[128:131] offset:32768
	ds_write_b128 v191, v[120:123] offset:33280
	ds_write_b128 v191, v[104:107] offset:33792
	ds_write_b128 v191, v[100:103] offset:34304
	ds_read2_b32 v[198:199], v153 offset0:26 offset1:27
	ds_read2_b32 v[208:209], v153 offset0:24 offset1:25
	ds_read2_b32 v[210:211], v153 offset0:18 offset1:19
	ds_read2_b32 v[212:213], v153 offset0:16 offset1:17
	ds_read2_b32 v[214:215], v153 offset0:10 offset1:11
	ds_read2_b32 v[216:217], v153 offset0:8 offset1:9
	ds_read2_b32 v[218:219], v153 offset0:2 offset1:3
	ds_read2_b32 v[220:221], v153 offset1:1
	s_andn2_b64 vcc, exec, s[82:83]
	v_mfma_f32_32x32x16_bf16 v[52:67], v[140:143], v[116:119], v[52:67]
	v_mfma_f32_32x32x16_bf16 v[52:67], v[136:139], v[112:115], v[52:67]
	v_mfma_f32_32x32x16_bf16 v[52:67], v[132:135], v[108:111], v[52:67]
	s_cbranch_vccnz .Lband_nopf
	v_mov_b32_e32 v205, 0
	v_lshlrev_b32_e32 v204, s47, v180
	v_add_u32_e32 v204, s56, v204
	v_mul_u32_u24_e32 v204, s5, v204
	v_lshl_add_u64 v[206:207], v[204:205], 0, v[156:157]
	global_load_dwordx4 v[144:147], v[206:207], off
	global_load_dwordx4 v[140:143], v[206:207], off offset:32
	global_load_dwordx4 v[136:139], v[206:207], off offset:64
	global_load_dwordx4 v[132:135], v[206:207], off offset:96
	v_lshlrev_b32_e32 v204, s47, v178
	v_add_u32_e32 v204, s56, v204
	v_mul_u32_u24_e32 v204, s5, v204
	v_lshl_add_u64 v[206:207], v[204:205], 0, v[158:159]
	global_load_dwordx4 v[128:131], v[206:207], off
	v_lshlrev_b32_e32 v204, s47, v176
	v_add_u32_e32 v204, s56, v204
	v_mul_u32_u24_e32 v204, s5, v204
	v_lshl_add_u64 v[206:207], v[204:205], 0, v[158:159]
	global_load_dwordx4 v[120:123], v[206:207], off
	v_lshlrev_b32_e32 v204, s47, v174
	v_add_u32_e32 v204, s56, v204
	v_mul_u32_u24_e32 v204, s5, v204
	v_lshl_add_u64 v[206:207], v[204:205], 0, v[158:159]
	global_load_dwordx4 v[104:107], v[206:207], off
	v_lshlrev_b32_e32 v204, s47, v172
	v_add_u32_e32 v204, s56, v204
	v_mul_u32_u24_e32 v204, s5, v204
	v_lshl_add_u64 v[206:207], v[204:205], 0, v[158:159]
	global_load_dwordx4 v[100:103], v[206:207], off
.Lband_nopf:
	s_waitcnt lgkmcnt(0)
	s_nop 10
	v_fmamk_f32 v197, v52, 0x3e38aa3b, v199
	v_fmac_f32_e32 v198, 0x3e38aa3b, v53
	v_max3_f32 v195, v197, s33, v198
	v_fmamk_f32 v53, v54, 0x3e38aa3b, v209
	v_fmamk_f32 v52, v55, 0x3e38aa3b, v208
	v_max3_f32 v195, v195, v53, v52
	v_fmamk_f32 v55, v56, 0x3e38aa3b, v211
	v_fmamk_f32 v54, v57, 0x3e38aa3b, v210
	v_max3_f32 v195, v195, v55, v54
	v_fmamk_f32 v57, v58, 0x3e38aa3b, v213
	v_fmamk_f32 v56, v59, 0x3e38aa3b, v212
	v_max3_f32 v195, v195, v57, v56
	v_fmamk_f32 v59, v60, 0x3e38aa3b, v215
	v_fmamk_f32 v58, v61, 0x3e38aa3b, v214
	v_max3_f32 v195, v195, v59, v58
	v_fmamk_f32 v61, v62, 0x3e38aa3b, v217
	v_fmamk_f32 v60, v63, 0x3e38aa3b, v216
	v_max3_f32 v195, v195, v61, v60
	v_fmamk_f32 v63, v64, 0x3e38aa3b, v219
	v_fmamk_f32 v62, v65, 0x3e38aa3b, v218
	v_max3_f32 v195, v195, v63, v62
	v_fmamk_f32 v65, v66, 0x3e38aa3b, v221
	v_fmamk_f32 v64, v67, 0x3e38aa3b, v220
	v_max3_f32 v66, v195, v65, v64
	v_mov_b32_e32 v67, v66
	s_nop 1
	v_permlane32_swap_b32_e32 v66, v67
	v_max3_f32 v195, v196, v66, v67
	v_sub_f32_e32 v67, v197, v195
	v_exp_f32_e32 v67, v67
	v_sub_f32_e32 v197, v198, v195
	v_exp_f32_e32 v197, v197
	v_sub_f32_e32 v53, v53, v195
	v_exp_f32_e32 v53, v53
	v_sub_f32_e32 v52, v52, v195
	v_exp_f32_e32 v52, v52
	v_sub_f32_e32 v55, v55, v195
	v_sub_f32_e32 v66, v196, v195
	v_add_f32_e32 v196, 0, v67
	v_exp_f32_e32 v55, v55
	v_sub_f32_e32 v54, v54, v195
	v_add_f32_e32 v196, v197, v196
	v_exp_f32_e32 v54, v54
	v_sub_f32_e32 v57, v57, v195
	v_add_f32_e32 v196, v53, v196
	v_exp_f32_e32 v198, v57
	v_add_f32_e32 v196, v52, v196
	v_add_f32_e32 v196, v55, v196
	v_add_f32_e32 v196, v54, v196
	v_sub_f32_e32 v56, v56, v195
	v_add_f32_e32 v57, v198, v196
	v_exp_f32_e32 v196, v56
	s_nop 0
	v_add_f32_e32 v56, v196, v57
	v_sub_f32_e32 v57, v59, v195
	v_exp_f32_e32 v59, v57
	v_sub_f32_e32 v57, v58, v195
	v_exp_f32_e32 v199, v57
	v_sub_f32_e32 v57, v61, v195
	v_exp_f32_e32 v200, v57
	v_sub_f32_e32 v57, v60, v195
	v_exp_f32_e32 v201, v57
	v_sub_f32_e32 v57, v63, v195
	v_add_f32_e32 v56, v59, v56
	v_exp_f32_e32 v202, v57
	v_sub_f32_e32 v57, v62, v195
	v_add_f32_e32 v56, v199, v56
	v_exp_f32_e32 v203, v57
	v_sub_f32_e32 v57, v65, v195
	v_add_f32_e32 v56, v200, v56
	v_exp_f32_e32 v65, v57
	v_sub_f32_e32 v57, v64, v195
	v_add_f32_e32 v56, v201, v56
	v_exp_f32_e32 v64, v57
	v_add_f32_e32 v56, v202, v56
	v_add_f32_e32 v56, v203, v56
	v_add_f32_e32 v56, v65, v56
	v_add_f32_e32 v57, v64, v56
	v_exp_f32_e32 v56, v66
	v_cvt_pk_bf16_f32 v60, v67, v197
	v_cvt_pk_bf16_f32 v62, v55, v54
	v_cvt_pk_bf16_f32 v55, v65, v64
	ds_read_b64_tr_b16 v[64:65], v192 offset:32768
	ds_read_b64_tr_b16 v[66:67], v192 offset:33280
	ds_read_b64_tr_b16 v[208:209], v192 offset:33792
	ds_read_b64_tr_b16 v[210:211], v192 offset:34304
	ds_read_b64_tr_b16 v[212:213], v192 offset:34816
	ds_read_b64_tr_b16 v[214:215], v192 offset:35328
	ds_read_b64_tr_b16 v[216:217], v192 offset:35840
	ds_read_b64_tr_b16 v[218:219], v192 offset:36352
	v_mov_b32_e32 v58, v57
	s_nop 1
	v_permlane32_swap_b32_e32 v57, v58
	v_pk_mul_f32 v[34:35], v[34:35], v[56:57] op_sel_hi:[1,0]
	v_pk_mul_f32 v[32:33], v[32:33], v[56:57] op_sel_hi:[1,0]
	v_pk_mul_f32 v[30:31], v[30:31], v[56:57] op_sel_hi:[1,0]
	v_pk_mul_f32 v[28:29], v[28:29], v[56:57] op_sel_hi:[1,0]
	v_pk_mul_f32 v[26:27], v[26:27], v[56:57] op_sel_hi:[1,0]
	v_pk_mul_f32 v[24:25], v[24:25], v[56:57] op_sel_hi:[1,0]
	v_pk_mul_f32 v[22:23], v[22:23], v[56:57] op_sel_hi:[1,0]
	v_pk_mul_f32 v[20:21], v[20:21], v[56:57] op_sel_hi:[1,0]
	v_cvt_pk_bf16_f32 v61, v53, v52
	v_cvt_pk_bf16_f32 v63, v198, v196
	v_cvt_pk_bf16_f32 v52, v59, v199
	v_cvt_pk_bf16_f32 v53, v200, v201
	v_cvt_pk_bf16_f32 v54, v202, v203
	v_pk_mul_f32 v[50:51], v[50:51], v[56:57] op_sel_hi:[1,0]
	s_waitcnt lgkmcnt(6)
	v_mfma_f32_32x32x16_bf16 v[20:35], v[64:67], v[60:63], v[20:35]
	v_mul_f32_e64 v48, v48, v56
	v_mul_f32_e64 v49, v49, v56
	v_mul_f32_e64 v46, v46, v56
	v_mul_f32_e64 v47, v47, v56
	v_pk_mul_f32 v[44:45], v[44:45], v[56:57] op_sel_hi:[1,0]
	v_pk_mul_f32 v[42:43], v[42:43], v[56:57] op_sel_hi:[1,0]
	v_pk_mul_f32 v[40:41], v[40:41], v[56:57] op_sel_hi:[1,0]
	v_pk_mul_f32 v[38:39], v[38:39], v[56:57] op_sel_hi:[1,0]
	s_waitcnt lgkmcnt(4)
	v_mfma_f32_32x32x16_bf16 v[20:35], v[208:211], v[52:55], v[20:35]
	v_mul_f32_e64 v36, v36, v56
	v_mul_f32_e64 v37, v37, v56
	s_waitcnt lgkmcnt(2)
	s_nop 0
	v_mfma_f32_32x32x16_bf16 v[36:51], v[212:215], v[60:63], v[36:51]
	s_waitcnt lgkmcnt(0)
	v_mfma_f32_32x32x16_bf16 v[36:51], v[216:219], v[52:55], v[36:51]
.LBB0_1267:
	v_add_f32_e32 v197, v57, v58
	v_fmac_f32_e32 v197, v194, v56
	s_add_i32 s41, s41, -1
	v_add_u32_e32 v172, s96, v172
	v_add_u32_e32 v174, s96, v174
	v_add_u32_e32 v176, s96, v176
	v_add_u32_e32 v178, s96, v178
	v_add_u32_e32 v180, s96, v180
	v_add_u32_e32 v153, 0x80, v153
	s_and_b64 vcc, exec, s[60:61]
	s_cbranch_vccnz .LBB0_1269
	v_mov_b32_e32 v196, v195
	v_mov_b32_e32 v194, v197
	s_branch .LBB0_1259
